# scatter: both per-expert prefix loops issue all 16 counter loads at once (masked sum) instead of two loads per serialized iteration
# speedup vs baseline: 1.0149x; 1.0099x over previous
.LBB0_1830:
	s_andn2_b64 vcc, exec, s[0:1]
	s_cbranch_vccnz .LBB0_1927
	v_readlane_b32 s0, v251, 1
	v_readlane_b32 s2, v251, 10
	v_readlane_b32 s1, v251, 2
	v_readlane_b32 s3, v251, 11
	s_load_dword s24, s[2:3], 0x0
	v_readlane_b32 s25, v251, 0
	s_load_dwordx2 s[2:3], s[0:1], 0x108
	v_readlane_b32 s0, v251, 12
	s_waitcnt lgkmcnt(0)
	s_mov_b32 s26, s24
	s_waitcnt vmcnt(9)
	v_mbcnt_lo_u32_b32 v13, -1, 0
	v_mbcnt_hi_u32_b32 v13, -1, v13
	s_add_u32 s6, s2, 0x556e4800
	v_add_u32_e32 v2, s0, v13
	v_ashrrev_i32_e32 v4, 5, v2
	s_movk_i32 s0, 0x100
	s_addc_u32 s7, s3, 0
	v_and_b32_e32 v0, 31, v13
	v_cmp_gt_i32_e32 vcc, s0, v4
	v_mov_b32_e32 v3, 0
	s_and_saveexec_b64 s[4:5], vcc
	s_cbranch_execz .LBB0_1843
	v_lshlrev_b32_e32 v46, 2, v2
	global_load_dword v47, v46, s[6:7]
	global_load_dword v48, v46, s[6:7] offset:2048
	v_add_u32_e32 v70, 0x1000, v46
	global_load_dword v49, v70, s[6:7]
	global_load_dword v50, v70, s[6:7] offset:2048
	v_add_u32_e32 v71, 0x2000, v46
	global_load_dword v51, v71, s[6:7]
	global_load_dword v52, v71, s[6:7] offset:2048
	v_add_u32_e32 v72, 0x3000, v46
	global_load_dword v53, v72, s[6:7]
	global_load_dword v54, v72, s[6:7] offset:2048
	v_add_u32_e32 v73, 0x4000, v46
	global_load_dword v55, v73, s[6:7]
	global_load_dword v56, v73, s[6:7] offset:2048
	v_add_u32_e32 v74, 0x5000, v46
	global_load_dword v57, v74, s[6:7]
	global_load_dword v58, v74, s[6:7] offset:2048
	v_add_u32_e32 v75, 0x6000, v46
	global_load_dword v59, v75, s[6:7]
	global_load_dword v60, v75, s[6:7] offset:2048
	v_add_u32_e32 v76, 0x7000, v46
	global_load_dword v61, v76, s[6:7]
	global_load_dword v62, v76, s[6:7] offset:2048
	s_waitcnt vmcnt(0)
	v_add3_u32 v3, v47, v48, v49
	v_add3_u32 v3, v3, v50, v51
	v_add3_u32 v3, v3, v52, v53
	v_add3_u32 v3, v3, v54, v55
	v_add3_u32 v3, v3, v56, v57
	v_add3_u32 v3, v3, v58, v59
	v_add3_u32 v3, v3, v60, v61
	v_add_u32_e32 v3, v3, v62

.LBB0_1861:
	v_cmp_gt_i32_e64 s[2:3], s25, v4
	v_mov_b32_e32 v13, 0
	s_barrier
	s_and_saveexec_b64 s[16:17], s[2:3]
	s_cbranch_execz .LBB0_1873
	v_lshlrev_b32_e32 v46, 2, v2
	global_load_dword v47, v46, s[6:7]
	global_load_dword v48, v46, s[6:7] offset:2048
	v_add_u32_e32 v70, 0x1000, v46
	global_load_dword v49, v70, s[6:7]
	global_load_dword v50, v70, s[6:7] offset:2048
	v_add_u32_e32 v71, 0x2000, v46
	global_load_dword v51, v71, s[6:7]
	global_load_dword v52, v71, s[6:7] offset:2048
	v_add_u32_e32 v72, 0x3000, v46
	global_load_dword v53, v72, s[6:7]
	global_load_dword v54, v72, s[6:7] offset:2048
	v_add_u32_e32 v73, 0x4000, v46
	global_load_dword v55, v73, s[6:7]
	global_load_dword v56, v73, s[6:7] offset:2048
	v_add_u32_e32 v74, 0x5000, v46
	global_load_dword v57, v74, s[6:7]
	global_load_dword v58, v74, s[6:7] offset:2048
	v_add_u32_e32 v75, 0x6000, v46
	global_load_dword v59, v75, s[6:7]
	global_load_dword v60, v75, s[6:7] offset:2048
	v_add_u32_e32 v76, 0x7000, v46
	global_load_dword v61, v76, s[6:7]
	global_load_dword v62, v76, s[6:7] offset:2048
	v_sub_u32_e32 v77, s25, v4
	v_add_u32_e32 v77, 15, v77
	v_lshrrev_b32_e32 v77, 4, v77
	s_waitcnt vmcnt(0)
	v_mov_b32_e32 v13, 0
	v_cmp_lt_u32_e64 s[28:29], 0, v77
	v_cmp_lt_u32_e64 s[30:31], 1, v77
	v_cmp_lt_u32_e64 s[34:35], 2, v77
	v_cmp_lt_u32_e64 s[36:37], 3, v77
	v_cndmask_b32_e64 v47, 0, v47, s[28:29]
	v_cndmask_b32_e64 v48, 0, v48, s[30:31]
	v_cndmask_b32_e64 v49, 0, v49, s[34:35]
	v_cndmask_b32_e64 v50, 0, v50, s[36:37]
	v_add3_u32 v13, v13, v47, v48
	v_add3_u32 v13, v13, v49, v50
	v_cmp_lt_u32_e64 s[28:29], 4, v77
	v_cmp_lt_u32_e64 s[30:31], 5, v77
	v_cmp_lt_u32_e64 s[34:35], 6, v77
	v_cmp_lt_u32_e64 s[36:37], 7, v77
	v_cndmask_b32_e64 v51, 0, v51, s[28:29]
	v_cndmask_b32_e64 v52, 0, v52, s[30:31]
	v_cndmask_b32_e64 v53, 0, v53, s[34:35]
	v_cndmask_b32_e64 v54, 0, v54, s[36:37]
	v_add3_u32 v13, v13, v51, v52
	v_add3_u32 v13, v13, v53, v54
	v_cmp_lt_u32_e64 s[28:29], 8, v77
	v_cmp_lt_u32_e64 s[30:31], 9, v77
	v_cmp_lt_u32_e64 s[34:35], 10, v77
	v_cmp_lt_u32_e64 s[36:37], 11, v77
	v_cndmask_b32_e64 v55, 0, v55, s[28:29]
	v_cndmask_b32_e64 v56, 0, v56, s[30:31]
	v_cndmask_b32_e64 v57, 0, v57, s[34:35]
	v_cndmask_b32_e64 v58, 0, v58, s[36:37]
	v_add3_u32 v13, v13, v55, v56
	v_add3_u32 v13, v13, v57, v58
	v_cmp_lt_u32_e64 s[28:29], 12, v77
	v_cmp_lt_u32_e64 s[30:31], 13, v77
	v_cmp_lt_u32_e64 s[34:35], 14, v77
	v_cmp_lt_u32_e64 s[36:37], 15, v77
	v_cndmask_b32_e64 v59, 0, v59, s[28:29]
	v_cndmask_b32_e64 v60, 0, v60, s[30:31]
	v_cndmask_b32_e64 v61, 0, v61, s[34:35]
	v_cndmask_b32_e64 v62, 0, v62, s[36:37]
	v_add3_u32 v13, v13, v59, v60
	v_add3_u32 v13, v13, v61, v62
